# baseline (speedup 1.0000x reference)
.Lq2_nd0_1:
	v_mfma_scale_f32_32x32x64_f8f6f4 v[18:33], v[66:73], v[146:153], 0, v203, v203 op_sel_hi:[0,0,0]
	v_exp_f32_e64 v2, -v2
	v_exp_f32_e64 v3, -v3
	v_exp_f32_e64 v4, -v4
	v_exp_f32_e64 v5, -v5
	s_waitcnt lgkmcnt(0)
	v_add_co_u32_e64 v200, s[42:43], v200, v200
	v_add_co_u32_e64 v200, s[48:49], v200, v200
	v_add_co_u32_e64 v200, s[50:51], v200, v200
	v_add_co_u32_e64 v200, s[56:57], v200, v200
	v_pk_add_f32 v[2:3], v[2:3], v[162:163]
	v_pk_add_f32 v[4:5], v[4:5], v[164:165]
	v_cndmask_b32_e64 v2, 1.0, v2, s[42:43]
	v_cndmask_b32_e64 v3, 1.0, v3, s[48:49]
	v_cndmask_b32_e64 v4, 1.0, v4, s[50:51]
	v_cndmask_b32_e64 v5, 1.0, v5, s[56:57]
	v_pk_mul_f32 v[204:205], v[204:205], v[2:3]
	v_pk_mul_f32 v[206:207], v[206:207], v[4:5]
	v_mfma_scale_f32_32x32x64_f8f6f4 v[18:33], v[74:81], v[154:161], v[18:33], v203, v203 op_sel_hi:[0,0,0]
	v_exp_f32_e64 v6, -v6
	v_exp_f32_e64 v7, -v7
	v_exp_f32_e64 v8, -v8
	v_exp_f32_e64 v9, -v9
	v_add_co_u32_e64 v200, s[42:43], v200, v200
	v_add_co_u32_e64 v200, s[48:49], v200, v200
	v_add_co_u32_e64 v200, s[50:51], v200, v200
	v_add_co_u32_e64 v200, s[56:57], v200, v200
	v_pk_add_f32 v[6:7], v[6:7], v[166:167]
	v_pk_add_f32 v[8:9], v[8:9], v[168:169]
	v_cndmask_b32_e64 v6, 1.0, v6, s[42:43]
	v_cndmask_b32_e64 v7, 1.0, v7, s[48:49]
	v_cndmask_b32_e64 v8, 1.0, v8, s[50:51]
	v_cndmask_b32_e64 v9, 1.0, v9, s[56:57]
	v_pk_mul_f32 v[208:209], v[208:209], v[6:7]
	v_pk_mul_f32 v[210:211], v[210:211], v[8:9]
	v_mfma_scale_f32_32x32x64_f8f6f4 v[18:33], v[82:89], v[138:145], v[18:33], v203, v203 op_sel_hi:[0,0,0]
	v_exp_f32_e64 v10, -v10
	v_exp_f32_e64 v11, -v11
	v_exp_f32_e64 v12, -v12
	v_exp_f32_e64 v13, -v13
	v_add_co_u32_e64 v200, s[42:43], v200, v200
	v_add_co_u32_e64 v200, s[48:49], v200, v200
	v_add_co_u32_e64 v200, s[50:51], v200, v200
	v_add_co_u32_e64 v200, s[56:57], v200, v200
	v_pk_add_f32 v[10:11], v[10:11], v[170:171]
	v_pk_add_f32 v[12:13], v[12:13], v[172:173]
	v_cndmask_b32_e64 v10, 1.0, v10, s[42:43]
	v_cndmask_b32_e64 v11, 1.0, v11, s[48:49]
	v_cndmask_b32_e64 v12, 1.0, v12, s[50:51]
	v_cndmask_b32_e64 v13, 1.0, v13, s[56:57]
	v_pk_mul_f32 v[212:213], v[212:213], v[10:11]
	v_pk_mul_f32 v[214:215], v[214:215], v[12:13]
	v_mfma_scale_f32_32x32x64_f8f6f4 v[18:33], v[90:97], v[130:137], v[18:33], v203, v203 op_sel_hi:[0,0,0]
	v_exp_f32_e64 v14, -v14
	v_exp_f32_e64 v15, -v15
	v_exp_f32_e64 v16, -v16
	v_exp_f32_e64 v17, -v17
	v_add_co_u32_e64 v200, s[42:43], v200, v200
	v_add_co_u32_e64 v200, s[48:49], v200, v200
	v_add_co_u32_e64 v200, s[50:51], v200, v200
	v_add_co_u32_e64 v200, s[56:57], v200, v200
	v_pk_add_f32 v[14:15], v[14:15], v[174:175]
	v_pk_add_f32 v[16:17], v[16:17], v[176:177]
	v_cndmask_b32_e64 v14, 1.0, v14, s[42:43]
	v_cndmask_b32_e64 v15, 1.0, v15, s[48:49]
	v_cndmask_b32_e64 v16, 1.0, v16, s[50:51]
	v_cndmask_b32_e64 v17, 1.0, v17, s[56:57]
	v_pk_mul_f32 v[216:217], v[216:217], v[14:15]
	v_pk_mul_f32 v[218:219], v[218:219], v[16:17]
	s_cmp_lg_u32 s55, s40
	s_cbranch_scc1 .Lq2_nd1_1
	s_nop 15
	s_nop 7
	v_cndmask_b32_e64 v18, v18, v199, s[0:1]
	v_cndmask_b32_e64 v19, v19, v199, s[2:3]
	v_cndmask_b32_e64 v20, v20, v199, s[4:5]
	v_cndmask_b32_e64 v21, v21, v199, s[6:7]
	v_cndmask_b32_e64 v22, v22, v199, s[8:9]
	v_cndmask_b32_e64 v23, v23, v199, s[10:11]
	v_cndmask_b32_e64 v24, v24, v199, s[12:13]
	v_cndmask_b32_e64 v25, v25, v199, s[14:15]
	v_cndmask_b32_e64 v26, v26, v199, s[16:17]
	v_cndmask_b32_e64 v27, v27, v199, s[18:19]
	v_cndmask_b32_e64 v28, v28, v199, s[20:21]
	v_cndmask_b32_e64 v29, v29, v199, s[22:23]
	v_cndmask_b32_e64 v30, v30, v199, s[24:25]
	v_cndmask_b32_e64 v31, v31, v199, s[26:27]
	v_cndmask_b32_e64 v32, v32, v199, s[28:29]
	v_cndmask_b32_e64 v33, v33, v199, s[30:31]
.Lq2_nd1_1:
	s_nop 3
	s_waitcnt vmcnt(6)
	v_mfma_scale_f32_32x32x64_f8f6f4 v[2:17], v[34:41], v[106:113], 0, v203, v203 op_sel_hi:[0,0,0]
	v_exp_f32_e64 v18, -v18
	v_exp_f32_e64 v19, -v19
	v_exp_f32_e64 v20, -v20
	v_exp_f32_e64 v21, -v21
	v_add_co_u32_e64 v200, s[42:43], v200, v200
	v_add_co_u32_e64 v200, s[48:49], v200, v200
	v_add_co_u32_e64 v200, s[50:51], v200, v200
	v_add_co_u32_e64 v200, s[56:57], v200, v200
	v_pk_add_f32 v[18:19], v[18:19], v[178:179]
	v_pk_add_f32 v[20:21], v[20:21], v[180:181]
	v_cndmask_b32_e64 v18, 1.0, v18, s[42:43]
	v_cndmask_b32_e64 v19, 1.0, v19, s[48:49]
	v_cndmask_b32_e64 v20, 1.0, v20, s[50:51]
	v_cndmask_b32_e64 v21, 1.0, v21, s[56:57]
	v_pk_mul_f32 v[220:221], v[220:221], v[18:19]
	v_pk_mul_f32 v[222:223], v[222:223], v[20:21]
	s_waitcnt vmcnt(4)
	v_mfma_scale_f32_32x32x64_f8f6f4 v[2:17], v[42:49], v[122:129], v[2:17], v203, v203 op_sel_hi:[0,0,0]
	v_exp_f32_e64 v22, -v22
	v_exp_f32_e64 v23, -v23
	v_exp_f32_e64 v24, -v24
	v_exp_f32_e64 v25, -v25
	v_add_co_u32_e64 v200, s[42:43], v200, v200
	v_add_co_u32_e64 v200, s[48:49], v200, v200
	v_add_co_u32_e64 v200, s[50:51], v200, v200
	v_add_co_u32_e64 v200, s[56:57], v200, v200
	v_pk_add_f32 v[22:23], v[22:23], v[182:183]
	v_pk_add_f32 v[24:25], v[24:25], v[184:185]
	v_cndmask_b32_e64 v22, 1.0, v22, s[42:43]
	v_cndmask_b32_e64 v23, 1.0, v23, s[48:49]
	v_cndmask_b32_e64 v24, 1.0, v24, s[50:51]
	v_cndmask_b32_e64 v25, 1.0, v25, s[56:57]
	v_pk_mul_f32 v[224:225], v[224:225], v[22:23]
	v_pk_mul_f32 v[226:227], v[226:227], v[24:25]
	s_waitcnt vmcnt(2)
	v_mfma_scale_f32_32x32x64_f8f6f4 v[2:17], v[50:57], v[114:121], v[2:17], v203, v203 op_sel_hi:[0,0,0]
	v_exp_f32_e64 v26, -v26
	v_exp_f32_e64 v27, -v27
	v_exp_f32_e64 v28, -v28
	v_exp_f32_e64 v29, -v29
	v_add_co_u32_e64 v200, s[42:43], v200, v200
	v_add_co_u32_e64 v200, s[48:49], v200, v200
	v_add_co_u32_e64 v200, s[50:51], v200, v200
	v_add_co_u32_e64 v200, s[56:57], v200, v200
	v_pk_add_f32 v[26:27], v[26:27], v[186:187]
	v_pk_add_f32 v[28:29], v[28:29], v[188:189]
	v_cndmask_b32_e64 v26, 1.0, v26, s[42:43]
	v_cndmask_b32_e64 v27, 1.0, v27, s[48:49]
	v_cndmask_b32_e64 v28, 1.0, v28, s[50:51]
	v_cndmask_b32_e64 v29, 1.0, v29, s[56:57]
	v_pk_mul_f32 v[228:229], v[228:229], v[26:27]
	v_pk_mul_f32 v[230:231], v[230:231], v[28:29]
	s_waitcnt vmcnt(0)
	v_mfma_scale_f32_32x32x64_f8f6f4 v[2:17], v[58:65], v[98:105], v[2:17], v203, v203 op_sel_hi:[0,0,0]
	v_exp_f32_e64 v30, -v30
	v_exp_f32_e64 v31, -v31
	v_exp_f32_e64 v32, -v32
	v_exp_f32_e64 v33, -v33
	v_add_co_u32_e64 v200, s[42:43], v200, v200
	v_add_co_u32_e64 v200, s[48:49], v200, v200
	v_add_co_u32_e64 v200, s[50:51], v200, v200
	v_add_co_u32_e64 v200, s[56:57], v200, v200
	v_pk_add_f32 v[30:31], v[30:31], v[190:191]
	v_pk_add_f32 v[32:33], v[32:33], v[192:193]
	v_cndmask_b32_e64 v30, 1.0, v30, s[42:43]
	v_cndmask_b32_e64 v31, 1.0, v31, s[48:49]
	v_cndmask_b32_e64 v32, 1.0, v32, s[50:51]
	v_cndmask_b32_e64 v33, 1.0, v33, s[56:57]
	v_pk_mul_f32 v[232:233], v[232:233], v[30:31]
	v_pk_mul_f32 v[234:235], v[234:235], v[32:33]
	s_lshl_b32 s34, s39, 2
	s_add_i32 s34, s34, 2
	s_add_i32 s34, s34, s35
	s_and_b32 s41, s34, 15
	s_add_i32 s54, s34, 1
	s_and_b32 s54, s54, 15
	s_lshl_b32 s55, s41, 8
	s_lshl_b32 s38, s52, 12
	s_add_i32 s55, s55, s38
	v_lshl_add_u32 v236, v194, 2, s55
	ds_read_b32 v200, v236
	s_lshl_b32 s34, s54, 3
	s_add_i32 s34, s34, s52
	s_lshl_b32 s34, s34, 13
	s_add_i32 s34, s34, s53
	buffer_load_dwordx4 v[146:149], v195, s[44:47], s34 offen
	s_or_b32 s42, s34, 0x400
	buffer_load_dwordx4 v[150:153], v195, s[44:47], s42 offen
	s_or_b32 s43, s34, 0x800
	buffer_load_dwordx4 v[154:157], v195, s[44:47], s43 offen
	s_or_b32 s42, s34, 0xc00
	buffer_load_dwordx4 v[158:161], v195, s[44:47], s42 offen
	s_or_b32 s43, s34, 0x1000
	buffer_load_dwordx4 v[138:141], v195, s[44:47], s43 offen
	s_or_b32 s42, s34, 0x1400
	buffer_load_dwordx4 v[142:145], v195, s[44:47], s42 offen
	s_or_b32 s43, s34, 0x1800
	buffer_load_dwordx4 v[130:133], v195, s[44:47], s43 offen
	s_or_b32 s42, s34, 0x1c00
	buffer_load_dwordx4 v[134:137], v195, s[44:47], s42 offen
	s_lshl_b32 s55, s41, 3
	s_add_i32 s55, s55, s52
	s_cmp_lg_u32 s55, s33
	s_cbranch_scc1 .Lq2_nd0_2
	v_cndmask_b32_e64 v2, v2, v198, s[0:1]
	v_cndmask_b32_e64 v3, v3, v198, s[2:3]
	v_cndmask_b32_e64 v4, v4, v198, s[4:5]
	v_cndmask_b32_e64 v5, v5, v198, s[6:7]
	v_cndmask_b32_e64 v6, v6, v198, s[8:9]
	v_cndmask_b32_e64 v7, v7, v198, s[10:11]
	v_cndmask_b32_e64 v8, v8, v198, s[12:13]
	v_cndmask_b32_e64 v9, v9, v198, s[14:15]
	v_cndmask_b32_e64 v10, v10, v198, s[16:17]
	v_cndmask_b32_e64 v11, v11, v198, s[18:19]
	v_cndmask_b32_e64 v12, v12, v198, s[20:21]
	v_cndmask_b32_e64 v13, v13, v198, s[22:23]
	v_cndmask_b32_e64 v14, v14, v198, s[24:25]
	v_cndmask_b32_e64 v15, v15, v198, s[26:27]
	v_cndmask_b32_e64 v16, v16, v198, s[28:29]
	v_cndmask_b32_e64 v17, v17, v198, s[30:31]
.Lq2_nd0_2:
	v_mfma_scale_f32_32x32x64_f8f6f4 v[18:33], v[66:73], v[106:113], 0, v203, v203 op_sel_hi:[0,0,0]
	v_exp_f32_e64 v2, -v2
	v_exp_f32_e64 v3, -v3
	v_exp_f32_e64 v4, -v4
	v_exp_f32_e64 v5, -v5
	s_waitcnt lgkmcnt(0)
	v_add_co_u32_e64 v200, s[42:43], v200, v200
	v_add_co_u32_e64 v200, s[48:49], v200, v200
	v_add_co_u32_e64 v200, s[50:51], v200, v200
	v_add_co_u32_e64 v200, s[56:57], v200, v200
	v_pk_add_f32 v[2:3], v[2:3], v[162:163]
	v_pk_add_f32 v[4:5], v[4:5], v[164:165]
	v_cndmask_b32_e64 v2, 1.0, v2, s[42:43]
	v_cndmask_b32_e64 v3, 1.0, v3, s[48:49]
	v_cndmask_b32_e64 v4, 1.0, v4, s[50:51]
	v_cndmask_b32_e64 v5, 1.0, v5, s[56:57]
	v_pk_mul_f32 v[204:205], v[204:205], v[2:3]
	v_pk_mul_f32 v[206:207], v[206:207], v[4:5]
	v_mfma_scale_f32_32x32x64_f8f6f4 v[18:33], v[74:81], v[122:129], v[18:33], v203, v203 op_sel_hi:[0,0,0]
	v_exp_f32_e64 v6, -v6
	v_exp_f32_e64 v7, -v7
	v_exp_f32_e64 v8, -v8
	v_exp_f32_e64 v9, -v9
	v_add_co_u32_e64 v200, s[42:43], v200, v200
	v_add_co_u32_e64 v200, s[48:49], v200, v200
	v_add_co_u32_e64 v200, s[50:51], v200, v200
	v_add_co_u32_e64 v200, s[56:57], v200, v200
	v_pk_add_f32 v[6:7], v[6:7], v[166:167]
	v_pk_add_f32 v[8:9], v[8:9], v[168:169]
	v_cndmask_b32_e64 v6, 1.0, v6, s[42:43]
	v_cndmask_b32_e64 v7, 1.0, v7, s[48:49]
	v_cndmask_b32_e64 v8, 1.0, v8, s[50:51]
	v_cndmask_b32_e64 v9, 1.0, v9, s[56:57]
	v_pk_mul_f32 v[208:209], v[208:209], v[6:7]
	v_pk_mul_f32 v[210:211], v[210:211], v[8:9]
	v_mfma_scale_f32_32x32x64_f8f6f4 v[18:33], v[82:89], v[114:121], v[18:33], v203, v203 op_sel_hi:[0,0,0]
	v_exp_f32_e64 v10, -v10
	v_exp_f32_e64 v11, -v11
	v_exp_f32_e64 v12, -v12
	v_exp_f32_e64 v13, -v13
	v_add_co_u32_e64 v200, s[42:43], v200, v200
	v_add_co_u32_e64 v200, s[48:49], v200, v200
	v_add_co_u32_e64 v200, s[50:51], v200, v200
	v_add_co_u32_e64 v200, s[56:57], v200, v200
	v_pk_add_f32 v[10:11], v[10:11], v[170:171]
	v_pk_add_f32 v[12:13], v[12:13], v[172:173]
	v_cndmask_b32_e64 v10, 1.0, v10, s[42:43]
	v_cndmask_b32_e64 v11, 1.0, v11, s[48:49]
	v_cndmask_b32_e64 v12, 1.0, v12, s[50:51]
	v_cndmask_b32_e64 v13, 1.0, v13, s[56:57]
	v_pk_mul_f32 v[212:213], v[212:213], v[10:11]
	v_pk_mul_f32 v[214:215], v[214:215], v[12:13]
	v_mfma_scale_f32_32x32x64_f8f6f4 v[18:33], v[90:97], v[98:105], v[18:33], v203, v203 op_sel_hi:[0,0,0]
	v_exp_f32_e64 v14, -v14
	v_exp_f32_e64 v15, -v15
	v_exp_f32_e64 v16, -v16
	v_exp_f32_e64 v17, -v17
	v_add_co_u32_e64 v200, s[42:43], v200, v200
	v_add_co_u32_e64 v200, s[48:49], v200, v200
	v_add_co_u32_e64 v200, s[50:51], v200, v200
	v_add_co_u32_e64 v200, s[56:57], v200, v200
	v_pk_add_f32 v[14:15], v[14:15], v[174:175]
	v_pk_add_f32 v[16:17], v[16:17], v[176:177]
	v_cndmask_b32_e64 v14, 1.0, v14, s[42:43]
	v_cndmask_b32_e64 v15, 1.0, v15, s[48:49]
	v_cndmask_b32_e64 v16, 1.0, v16, s[50:51]
	v_cndmask_b32_e64 v17, 1.0, v17, s[56:57]
	v_pk_mul_f32 v[216:217], v[216:217], v[14:15]
	v_pk_mul_f32 v[218:219], v[218:219], v[16:17]
	s_cmp_lg_u32 s55, s40
	s_cbranch_scc1 .Lq2_nd1_2
	s_nop 15
	s_nop 7
	v_cndmask_b32_e64 v18, v18, v199, s[0:1]
	v_cndmask_b32_e64 v19, v19, v199, s[2:3]
	v_cndmask_b32_e64 v20, v20, v199, s[4:5]
	v_cndmask_b32_e64 v21, v21, v199, s[6:7]
	v_cndmask_b32_e64 v22, v22, v199, s[8:9]
	v_cndmask_b32_e64 v23, v23, v199, s[10:11]
	v_cndmask_b32_e64 v24, v24, v199, s[12:13]
	v_cndmask_b32_e64 v25, v25, v199, s[14:15]
	v_cndmask_b32_e64 v26, v26, v199, s[16:17]
	v_cndmask_b32_e64 v27, v27, v199, s[18:19]
	v_cndmask_b32_e64 v28, v28, v199, s[20:21]
	v_cndmask_b32_e64 v29, v29, v199, s[22:23]
	v_cndmask_b32_e64 v30, v30, v199, s[24:25]
	v_cndmask_b32_e64 v31, v31, v199, s[26:27]
	v_cndmask_b32_e64 v32, v32, v199, s[28:29]
	v_cndmask_b32_e64 v33, v33, v199, s[30:31]
.Lq2_nd1_2:
	s_nop 3
	s_waitcnt vmcnt(6)
	v_mfma_scale_f32_32x32x64_f8f6f4 v[2:17], v[34:41], v[146:153], 0, v203, v203 op_sel_hi:[0,0,0]
	v_exp_f32_e64 v18, -v18
	v_exp_f32_e64 v19, -v19
	v_exp_f32_e64 v20, -v20
	v_exp_f32_e64 v21, -v21
	v_add_co_u32_e64 v200, s[42:43], v200, v200
	v_add_co_u32_e64 v200, s[48:49], v200, v200
	v_add_co_u32_e64 v200, s[50:51], v200, v200
	v_add_co_u32_e64 v200, s[56:57], v200, v200
	v_pk_add_f32 v[18:19], v[18:19], v[178:179]
	v_pk_add_f32 v[20:21], v[20:21], v[180:181]
	v_cndmask_b32_e64 v18, 1.0, v18, s[42:43]
	v_cndmask_b32_e64 v19, 1.0, v19, s[48:49]
	v_cndmask_b32_e64 v20, 1.0, v20, s[50:51]
	v_cndmask_b32_e64 v21, 1.0, v21, s[56:57]
	v_pk_mul_f32 v[220:221], v[220:221], v[18:19]
	v_pk_mul_f32 v[222:223], v[222:223], v[20:21]
	s_waitcnt vmcnt(4)
	v_mfma_scale_f32_32x32x64_f8f6f4 v[2:17], v[42:49], v[154:161], v[2:17], v203, v203 op_sel_hi:[0,0,0]
	v_exp_f32_e64 v22, -v22
	v_exp_f32_e64 v23, -v23
	v_exp_f32_e64 v24, -v24
	v_exp_f32_e64 v25, -v25
	v_add_co_u32_e64 v200, s[42:43], v200, v200
	v_add_co_u32_e64 v200, s[48:49], v200, v200
	v_add_co_u32_e64 v200, s[50:51], v200, v200
	v_add_co_u32_e64 v200, s[56:57], v200, v200
	v_pk_add_f32 v[22:23], v[22:23], v[182:183]
	v_pk_add_f32 v[24:25], v[24:25], v[184:185]
	v_cndmask_b32_e64 v22, 1.0, v22, s[42:43]
	v_cndmask_b32_e64 v23, 1.0, v23, s[48:49]
	v_cndmask_b32_e64 v24, 1.0, v24, s[50:51]
	v_cndmask_b32_e64 v25, 1.0, v25, s[56:57]
	v_pk_mul_f32 v[224:225], v[224:225], v[22:23]
	v_pk_mul_f32 v[226:227], v[226:227], v[24:25]
	s_waitcnt vmcnt(2)
	v_mfma_scale_f32_32x32x64_f8f6f4 v[2:17], v[50:57], v[138:145], v[2:17], v203, v203 op_sel_hi:[0,0,0]
	v_exp_f32_e64 v26, -v26
	v_exp_f32_e64 v27, -v27
	v_exp_f32_e64 v28, -v28
	v_exp_f32_e64 v29, -v29
	v_add_co_u32_e64 v200, s[42:43], v200, v200
	v_add_co_u32_e64 v200, s[48:49], v200, v200
	v_add_co_u32_e64 v200, s[50:51], v200, v200
	v_add_co_u32_e64 v200, s[56:57], v200, v200
	v_pk_add_f32 v[26:27], v[26:27], v[186:187]
	v_pk_add_f32 v[28:29], v[28:29], v[188:189]
	v_cndmask_b32_e64 v26, 1.0, v26, s[42:43]
	v_cndmask_b32_e64 v27, 1.0, v27, s[48:49]
	v_cndmask_b32_e64 v28, 1.0, v28, s[50:51]
	v_cndmask_b32_e64 v29, 1.0, v29, s[56:57]
	v_pk_mul_f32 v[228:229], v[228:229], v[26:27]
	v_pk_mul_f32 v[230:231], v[230:231], v[28:29]
	s_waitcnt vmcnt(0)
	v_mfma_scale_f32_32x32x64_f8f6f4 v[2:17], v[58:65], v[130:137], v[2:17], v203, v203 op_sel_hi:[0,0,0]
	v_exp_f32_e64 v30, -v30
	v_exp_f32_e64 v31, -v31
	v_exp_f32_e64 v32, -v32
	v_exp_f32_e64 v33, -v33
	v_add_co_u32_e64 v200, s[42:43], v200, v200
	v_add_co_u32_e64 v200, s[48:49], v200, v200
	v_add_co_u32_e64 v200, s[50:51], v200, v200
	v_add_co_u32_e64 v200, s[56:57], v200, v200
	v_pk_add_f32 v[30:31], v[30:31], v[190:191]
	v_pk_add_f32 v[32:33], v[32:33], v[192:193]
	v_cndmask_b32_e64 v30, 1.0, v30, s[42:43]
	v_cndmask_b32_e64 v31, 1.0, v31, s[48:49]
	v_cndmask_b32_e64 v32, 1.0, v32, s[50:51]
	v_cndmask_b32_e64 v33, 1.0, v33, s[56:57]
	v_pk_mul_f32 v[232:233], v[232:233], v[30:31]
	v_pk_mul_f32 v[234:235], v[234:235], v[32:33]
	s_lshl_b32 s34, s39, 2
	s_add_i32 s34, s34, 3
	s_add_i32 s34, s34, s35
	s_and_b32 s41, s34, 15
	s_add_i32 s54, s34, 1
	s_and_b32 s54, s54, 15
	s_lshl_b32 s55, s41, 8
	s_lshl_b32 s38, s52, 12
	s_add_i32 s55, s55, s38
	v_lshl_add_u32 v236, v194, 2, s55
	ds_read_b32 v200, v236
	s_lshl_b32 s34, s54, 3
	s_add_i32 s34, s34, s52
	s_lshl_b32 s34, s34, 13
	s_add_i32 s34, s34, s53
	buffer_load_dwordx4 v[106:109], v195, s[44:47], s34 offen
	s_or_b32 s42, s34, 0x400
	buffer_load_dwordx4 v[110:113], v195, s[44:47], s42 offen
	s_or_b32 s43, s34, 0x800
	buffer_load_dwordx4 v[122:125], v195, s[44:47], s43 offen
	s_or_b32 s42, s34, 0xc00
	buffer_load_dwordx4 v[126:129], v195, s[44:47], s42 offen
	s_or_b32 s43, s34, 0x1000
	buffer_load_dwordx4 v[114:117], v195, s[44:47], s43 offen
	s_or_b32 s42, s34, 0x1400
	buffer_load_dwordx4 v[118:121], v195, s[44:47], s42 offen
	s_or_b32 s43, s34, 0x1800
	buffer_load_dwordx4 v[98:101], v195, s[44:47], s43 offen
	s_or_b32 s42, s34, 0x1c00
	buffer_load_dwordx4 v[102:105], v195, s[44:47], s42 offen
	s_lshl_b32 s55, s41, 3
	s_add_i32 s55, s55, s52
	s_cmp_lg_u32 s55, s33
	s_cbranch_scc1 .Lq2_nd0_3
	v_cndmask_b32_e64 v2, v2, v198, s[0:1]
	v_cndmask_b32_e64 v3, v3, v198, s[2:3]
	v_cndmask_b32_e64 v4, v4, v198, s[4:5]
	v_cndmask_b32_e64 v5, v5, v198, s[6:7]
	v_cndmask_b32_e64 v6, v6, v198, s[8:9]
	v_cndmask_b32_e64 v7, v7, v198, s[10:11]
	v_cndmask_b32_e64 v8, v8, v198, s[12:13]
	v_cndmask_b32_e64 v9, v9, v198, s[14:15]
	v_cndmask_b32_e64 v10, v10, v198, s[16:17]
	v_cndmask_b32_e64 v11, v11, v198, s[18:19]
	v_cndmask_b32_e64 v12, v12, v198, s[20:21]
	v_cndmask_b32_e64 v13, v13, v198, s[22:23]
	v_cndmask_b32_e64 v14, v14, v198, s[24:25]
	v_cndmask_b32_e64 v15, v15, v198, s[26:27]
	v_cndmask_b32_e64 v16, v16, v198, s[28:29]
	v_cndmask_b32_e64 v17, v17, v198, s[30:31]
.Lq2_nd0_3:
	v_mfma_scale_f32_32x32x64_f8f6f4 v[18:33], v[66:73], v[146:153], 0, v203, v203 op_sel_hi:[0,0,0]
	ds_read_b128 v[236:239], v202
	v_exp_f32_e64 v2, -v2
	v_exp_f32_e64 v3, -v3
	v_exp_f32_e64 v4, -v4
	v_exp_f32_e64 v5, -v5
	s_waitcnt lgkmcnt(1)
	v_add_co_u32_e64 v200, s[42:43], v200, v200
	v_add_co_u32_e64 v200, s[48:49], v200, v200
	v_add_co_u32_e64 v200, s[50:51], v200, v200
	v_add_co_u32_e64 v200, s[56:57], v200, v200
	v_pk_add_f32 v[2:3], v[2:3], v[162:163]
	v_pk_add_f32 v[4:5], v[4:5], v[164:165]
	v_cndmask_b32_e64 v2, 1.0, v2, s[42:43]
	v_cndmask_b32_e64 v3, 1.0, v3, s[48:49]
	v_cndmask_b32_e64 v4, 1.0, v4, s[50:51]
	v_cndmask_b32_e64 v5, 1.0, v5, s[56:57]
	v_pk_mul_f32 v[204:205], v[204:205], v[2:3]
	v_pk_mul_f32 v[206:207], v[206:207], v[4:5]
	v_log_f32_e32 v2, v204
	v_log_f32_e32 v3, v205
	v_log_f32_e32 v4, v206
	v_log_f32_e32 v5, v207
	s_waitcnt lgkmcnt(0)
	v_fmac_f32_e32 v201, v2, v236
	v_fmac_f32_e32 v201, v3, v237
	v_fmac_f32_e32 v201, v4, v238
	v_fmac_f32_e32 v201, v5, v239
	v_mfma_scale_f32_32x32x64_f8f6f4 v[18:33], v[74:81], v[154:161], v[18:33], v203, v203 op_sel_hi:[0,0,0]
	ds_read_b128 v[236:239], v202 offset:16
	v_exp_f32_e64 v6, -v6
	v_exp_f32_e64 v7, -v7
	v_exp_f32_e64 v8, -v8
	v_exp_f32_e64 v9, -v9
	v_add_co_u32_e64 v200, s[42:43], v200, v200
	v_add_co_u32_e64 v200, s[48:49], v200, v200
	v_add_co_u32_e64 v200, s[50:51], v200, v200
	v_add_co_u32_e64 v200, s[56:57], v200, v200
	v_pk_add_f32 v[6:7], v[6:7], v[166:167]
	v_pk_add_f32 v[8:9], v[8:9], v[168:169]
	v_cndmask_b32_e64 v6, 1.0, v6, s[42:43]
	v_cndmask_b32_e64 v7, 1.0, v7, s[48:49]
	v_cndmask_b32_e64 v8, 1.0, v8, s[50:51]
	v_cndmask_b32_e64 v9, 1.0, v9, s[56:57]
	v_pk_mul_f32 v[208:209], v[208:209], v[6:7]
	v_pk_mul_f32 v[210:211], v[210:211], v[8:9]
	v_log_f32_e32 v6, v208
	v_log_f32_e32 v7, v209
	v_log_f32_e32 v8, v210
	v_log_f32_e32 v9, v211
	s_waitcnt lgkmcnt(0)
	v_fmac_f32_e32 v201, v6, v236
	v_fmac_f32_e32 v201, v7, v237
	v_fmac_f32_e32 v201, v8, v238
	v_fmac_f32_e32 v201, v9, v239
	v_mfma_scale_f32_32x32x64_f8f6f4 v[18:33], v[82:89], v[138:145], v[18:33], v203, v203 op_sel_hi:[0,0,0]
	ds_read_b128 v[236:239], v202 offset:32
	v_exp_f32_e64 v10, -v10
	v_exp_f32_e64 v11, -v11
	v_exp_f32_e64 v12, -v12
	v_exp_f32_e64 v13, -v13
	v_add_co_u32_e64 v200, s[42:43], v200, v200
	v_add_co_u32_e64 v200, s[48:49], v200, v200
	v_add_co_u32_e64 v200, s[50:51], v200, v200
	v_add_co_u32_e64 v200, s[56:57], v200, v200
	v_pk_add_f32 v[10:11], v[10:11], v[170:171]
	v_pk_add_f32 v[12:13], v[12:13], v[172:173]
	v_cndmask_b32_e64 v10, 1.0, v10, s[42:43]
	v_cndmask_b32_e64 v11, 1.0, v11, s[48:49]
	v_cndmask_b32_e64 v12, 1.0, v12, s[50:51]
	v_cndmask_b32_e64 v13, 1.0, v13, s[56:57]
	v_pk_mul_f32 v[212:213], v[212:213], v[10:11]
	v_pk_mul_f32 v[214:215], v[214:215], v[12:13]
	v_log_f32_e32 v10, v212
	v_log_f32_e32 v11, v213
	v_log_f32_e32 v12, v214
	v_log_f32_e32 v13, v215
	s_waitcnt lgkmcnt(0)
	v_fmac_f32_e32 v201, v10, v236
	v_fmac_f32_e32 v201, v11, v237
	v_fmac_f32_e32 v201, v12, v238
	v_fmac_f32_e32 v201, v13, v239
	v_mfma_scale_f32_32x32x64_f8f6f4 v[18:33], v[90:97], v[130:137], v[18:33], v203, v203 op_sel_hi:[0,0,0]
	ds_read_b128 v[236:239], v202 offset:48
	v_exp_f32_e64 v14, -v14
	v_exp_f32_e64 v15, -v15
	v_exp_f32_e64 v16, -v16
	v_exp_f32_e64 v17, -v17
	v_add_co_u32_e64 v200, s[42:43], v200, v200
	v_add_co_u32_e64 v200, s[48:49], v200, v200
	v_add_co_u32_e64 v200, s[50:51], v200, v200
	v_add_co_u32_e64 v200, s[56:57], v200, v200
	v_pk_add_f32 v[14:15], v[14:15], v[174:175]
	v_pk_add_f32 v[16:17], v[16:17], v[176:177]
	v_cndmask_b32_e64 v14, 1.0, v14, s[42:43]
	v_cndmask_b32_e64 v15, 1.0, v15, s[48:49]
	v_cndmask_b32_e64 v16, 1.0, v16, s[50:51]
	v_cndmask_b32_e64 v17, 1.0, v17, s[56:57]
	v_pk_mul_f32 v[216:217], v[216:217], v[14:15]
	v_pk_mul_f32 v[218:219], v[218:219], v[16:17]
	v_log_f32_e32 v14, v216
	v_log_f32_e32 v15, v217
	v_log_f32_e32 v16, v218
	v_log_f32_e32 v17, v219
	s_waitcnt lgkmcnt(0)
	v_fmac_f32_e32 v201, v14, v236
	v_fmac_f32_e32 v201, v15, v237
	v_fmac_f32_e32 v201, v16, v238
	v_fmac_f32_e32 v201, v17, v239
	s_cmp_lg_u32 s55, s40
	s_cbranch_scc1 .Lq2_nd1_3
	s_nop 15
	s_nop 7
	v_cndmask_b32_e64 v18, v18, v199, s[0:1]
	v_cndmask_b32_e64 v19, v19, v199, s[2:3]
	v_cndmask_b32_e64 v20, v20, v199, s[4:5]
	v_cndmask_b32_e64 v21, v21, v199, s[6:7]
	v_cndmask_b32_e64 v22, v22, v199, s[8:9]
	v_cndmask_b32_e64 v23, v23, v199, s[10:11]
	v_cndmask_b32_e64 v24, v24, v199, s[12:13]
	v_cndmask_b32_e64 v25, v25, v199, s[14:15]
	v_cndmask_b32_e64 v26, v26, v199, s[16:17]
	v_cndmask_b32_e64 v27, v27, v199, s[18:19]
	v_cndmask_b32_e64 v28, v28, v199, s[20:21]
	v_cndmask_b32_e64 v29, v29, v199, s[22:23]
	v_cndmask_b32_e64 v30, v30, v199, s[24:25]
	v_cndmask_b32_e64 v31, v31, v199, s[26:27]
	v_cndmask_b32_e64 v32, v32, v199, s[28:29]
	v_cndmask_b32_e64 v33, v33, v199, s[30:31]
.Lq2_nd1_3:
	s_nop 3
	s_waitcnt vmcnt(6)
	v_mfma_scale_f32_32x32x64_f8f6f4 v[2:17], v[34:41], v[106:113], 0, v203, v203 op_sel_hi:[0,0,0]
	ds_read_b128 v[236:239], v202 offset:64
	v_exp_f32_e64 v18, -v18
	v_exp_f32_e64 v19, -v19
	v_exp_f32_e64 v20, -v20
	v_exp_f32_e64 v21, -v21
	v_add_co_u32_e64 v200, s[42:43], v200, v200
	v_add_co_u32_e64 v200, s[48:49], v200, v200
	v_add_co_u32_e64 v200, s[50:51], v200, v200
	v_add_co_u32_e64 v200, s[56:57], v200, v200
	v_pk_add_f32 v[18:19], v[18:19], v[178:179]
	v_pk_add_f32 v[20:21], v[20:21], v[180:181]
	v_cndmask_b32_e64 v18, 1.0, v18, s[42:43]
	v_cndmask_b32_e64 v19, 1.0, v19, s[48:49]
	v_cndmask_b32_e64 v20, 1.0, v20, s[50:51]
	v_cndmask_b32_e64 v21, 1.0, v21, s[56:57]
	v_pk_mul_f32 v[220:221], v[220:221], v[18:19]
	v_pk_mul_f32 v[222:223], v[222:223], v[20:21]
	v_log_f32_e32 v18, v220
	v_log_f32_e32 v19, v221
	v_log_f32_e32 v20, v222
	v_log_f32_e32 v21, v223
	s_waitcnt lgkmcnt(0)
	v_fmac_f32_e32 v201, v18, v236
	v_fmac_f32_e32 v201, v19, v237
	v_fmac_f32_e32 v201, v20, v238
	v_fmac_f32_e32 v201, v21, v239
	s_waitcnt vmcnt(4)
	v_mfma_scale_f32_32x32x64_f8f6f4 v[2:17], v[42:49], v[122:129], v[2:17], v203, v203 op_sel_hi:[0,0,0]
	ds_read_b128 v[236:239], v202 offset:80
	v_exp_f32_e64 v22, -v22
	v_exp_f32_e64 v23, -v23
	v_exp_f32_e64 v24, -v24
	v_exp_f32_e64 v25, -v25
	v_add_co_u32_e64 v200, s[42:43], v200, v200
	v_add_co_u32_e64 v200, s[48:49], v200, v200
	v_add_co_u32_e64 v200, s[50:51], v200, v200
	v_add_co_u32_e64 v200, s[56:57], v200, v200
	v_pk_add_f32 v[22:23], v[22:23], v[182:183]
	v_pk_add_f32 v[24:25], v[24:25], v[184:185]
	v_cndmask_b32_e64 v22, 1.0, v22, s[42:43]
	v_cndmask_b32_e64 v23, 1.0, v23, s[48:49]
	v_cndmask_b32_e64 v24, 1.0, v24, s[50:51]
	v_cndmask_b32_e64 v25, 1.0, v25, s[56:57]
	v_pk_mul_f32 v[224:225], v[224:225], v[22:23]
	v_pk_mul_f32 v[226:227], v[226:227], v[24:25]
	v_log_f32_e32 v22, v224
	v_log_f32_e32 v23, v225
	v_log_f32_e32 v24, v226
	v_log_f32_e32 v25, v227
	s_waitcnt lgkmcnt(0)
	v_fmac_f32_e32 v201, v22, v236
	v_fmac_f32_e32 v201, v23, v237
	v_fmac_f32_e32 v201, v24, v238
	v_fmac_f32_e32 v201, v25, v239
	s_waitcnt vmcnt(2)
	v_mfma_scale_f32_32x32x64_f8f6f4 v[2:17], v[50:57], v[114:121], v[2:17], v203, v203 op_sel_hi:[0,0,0]
	ds_read_b128 v[236:239], v202 offset:96
	v_exp_f32_e64 v26, -v26
	v_exp_f32_e64 v27, -v27
	v_exp_f32_e64 v28, -v28
	v_exp_f32_e64 v29, -v29
	v_add_co_u32_e64 v200, s[42:43], v200, v200
	v_add_co_u32_e64 v200, s[48:49], v200, v200
	v_add_co_u32_e64 v200, s[50:51], v200, v200
	v_add_co_u32_e64 v200, s[56:57], v200, v200
	v_pk_add_f32 v[26:27], v[26:27], v[186:187]
	v_pk_add_f32 v[28:29], v[28:29], v[188:189]
	v_cndmask_b32_e64 v26, 1.0, v26, s[42:43]
	v_cndmask_b32_e64 v27, 1.0, v27, s[48:49]
	v_cndmask_b32_e64 v28, 1.0, v28, s[50:51]
	v_cndmask_b32_e64 v29, 1.0, v29, s[56:57]
	v_pk_mul_f32 v[228:229], v[228:229], v[26:27]
	v_pk_mul_f32 v[230:231], v[230:231], v[28:29]
	v_log_f32_e32 v26, v228
	v_log_f32_e32 v27, v229
	v_log_f32_e32 v28, v230
	v_log_f32_e32 v29, v231
	s_waitcnt lgkmcnt(0)
	v_fmac_f32_e32 v201, v26, v236
	v_fmac_f32_e32 v201, v27, v237
	v_fmac_f32_e32 v201, v28, v238
	v_fmac_f32_e32 v201, v29, v239
	s_waitcnt vmcnt(0)
	v_mfma_scale_f32_32x32x64_f8f6f4 v[2:17], v[58:65], v[98:105], v[2:17], v203, v203 op_sel_hi:[0,0,0]
	ds_read_b128 v[236:239], v202 offset:112
	v_exp_f32_e64 v30, -v30
	v_exp_f32_e64 v31, -v31
	v_exp_f32_e64 v32, -v32
	v_exp_f32_e64 v33, -v33
	v_add_co_u32_e64 v200, s[42:43], v200, v200
	v_add_co_u32_e64 v200, s[48:49], v200, v200
	v_add_co_u32_e64 v200, s[50:51], v200, v200
	v_add_co_u32_e64 v200, s[56:57], v200, v200
	v_pk_add_f32 v[30:31], v[30:31], v[190:191]
	v_pk_add_f32 v[32:33], v[32:33], v[192:193]
	v_cndmask_b32_e64 v30, 1.0, v30, s[42:43]
	v_cndmask_b32_e64 v31, 1.0, v31, s[48:49]
	v_cndmask_b32_e64 v32, 1.0, v32, s[50:51]
	v_cndmask_b32_e64 v33, 1.0, v33, s[56:57]
	v_pk_mul_f32 v[232:233], v[232:233], v[30:31]
	v_pk_mul_f32 v[234:235], v[234:235], v[32:33]
	v_log_f32_e32 v30, v232
	v_log_f32_e32 v31, v233
	v_log_f32_e32 v32, v234
	v_log_f32_e32 v33, v235
	s_waitcnt lgkmcnt(0)
	v_fmac_f32_e32 v201, v30, v236
	v_fmac_f32_e32 v201, v31, v237
	v_fmac_f32_e32 v201, v32, v238
	v_fmac_f32_e32 v201, v33, v239
	s_add_i32 s39, s39, 1
	s_cmp_lt_u32 s39, 4
	s_cbranch_scc1 .Lq2_loop
